# final drain converts two tiles per iteration (16 loads in flight per workgroup); opportunistic points keep single tiles
# baseline (speedup 1.0000x reference)
; #define LAS __attribute__((address_space(3)))
; __device__ __forceinline__ void lds_barrier() { asm volatile("s_waitcnt lgkmcnt(0)" ::: "memory"); __builtin_amdgcn_s_barrier(); asm volatile("" ::: "memory"); }
; __device__ __forceinline__ void phase_prologue(const Args& a, LAS unsigned char* lds) {
;     ...
;         int r = u; const float* src; int ldn, nvalid, NT, mode = 0; bf16_t* dst;
;         if (r < CJ0) { src = a.in[I_EVIN]; ldn = 6144; nvalid = 6144; NT = 48; dst = (bf16_t*)(a.ws + WS_WIN0); }
;         else if ((r -= CJ0) < CJ1) { src = a.in[I_EVOUT]; ldn = 2048; nvalid = 2048; NT = 16; dst = (bf16_t*)(a.ws + WS_WOUT0); }
;         else if ((r -= CJ1) < CJ2) { src = a.in[I_ODIN]; ldn = 6176; nvalid = 6176; NT = 50; dst = (bf16_t*)(a.ws + WS_WIN1); }
;         else if ((r -= CJ2) < CJ3) { src = a.in[I_ODOUT]; ldn = 2048; nvalid = 2048; NT = 16; dst = (bf16_t*)(a.ws + WS_WOUT1); }
;         else { r -= CJ3; const int which = r / CJM; r -= which * CJM; const int mtx = r >> 8; r &= 255; ldn = 2048; nvalid = 2048; NT = 16;
;             if (which == 0) { src = a.in[I_WGATE] + (size_t)mtx * 2048 * 2048; dst = (bf16_t*)(a.ws + WS_WGU) + (size_t)mtx * 4096 * 2048; mode = 1; }
;             else if (which == 1) { src = a.in[I_WUP] + (size_t)mtx * 2048 * 2048; dst = (bf16_t*)(a.ws + WS_WGU) + (size_t)mtx * 4096 * 2048; mode = 2; }
;             else { src = a.in[I_WDOWN] + (size_t)mtx * 2048 * 2048; dst = (bf16_t*)(a.ws + WS_WDN) + (size_t)mtx * 2048 * 2048; } }
;         const int kt = r / NT, ntl = r % NT, k0 = kt * 128, n0 = ntl * 128;
;         const int drow0 = mode == 0 ? n0 : (ntl * 256 + (mode == 2 ? 128 : 0));
;         f32x4 v[8];
; #pragma unroll
;         for (int i = 0; i < 8; ++i) { const int id = tid + 512 * i, row = id >> 5, c4 = id & 31, n = n0 + c4 * 4;
;             v[i] = (f32x4){0.f, 0.f, 0.f, 0.f};
;             if (n < nvalid) v[i] = *(const f32x4*)(src + (size_t)(k0 + row) * ldn + n); }
; #pragma unroll
;         for (int i = 0; i < 8; ++i) { const int id = tid + 512 * i, row = id >> 5, c4 = id & 31;
;             LAS float* tp = tile + row * 129 + c4 * 4; tp[0] = v[i][0]; tp[1] = v[i][1]; tp[2] = v[i][2]; tp[3] = v[i][3]; }
;         lds_barrier();
.Lcvz_t0b:
	s_mov_b64 exec, s[34:35]
	s_lshr_b32 s36, s24, 12
	s_bfe_u32 s30, s24, 0x40008
	s_add_i32 s30, s30, 16
	s_lshl_b32 s30, s30, 24
	s_bfe_u32 s31, s24, 0x40004
	s_and_b32 s32, s24, 15
	v_readlane_b32 s26, v254, 43
	v_readlane_b32 s27, v254, 44
	s_cmp_lg_u32 s36, 0
	s_cselect_b32 s26, s40, s26
	s_cselect_b32 s27, s41, s27
	s_lshl_b32 s33, s31, 20
	s_add_i32 s33, s33, s30
	s_lshl_b32 s37, s32, 9
	s_add_i32 s33, s33, s37
	s_add_u32 s26, s26, s33
	s_addc_u32 s27, s27, 0
	v_readlane_b32 s28, v254, 25
	v_readlane_b32 s29, v254, 26
	s_lshl_b32 s33, s32, 20
	s_add_i32 s33, s33, s30
	s_lshl_b32 s37, s36, 19
	s_add_i32 s33, s33, s37
	s_lshl_b32 s37, s31, 8
	s_add_i32 s33, s33, s37
	s_add_u32 s28, s28, s33
	s_addc_u32 s29, s29, 0
	s_add_i32 s42, s24, 1
	s_cmpk_gt_u32 s42, 0x1fff
	s_cselect_b32 s42, s24, s42
	s_lshr_b32 s36, s42, 12
	s_bfe_u32 s30, s42, 0x40008
	s_add_i32 s30, s30, 16
	s_lshl_b32 s30, s30, 24
	s_bfe_u32 s31, s42, 0x40004
	s_and_b32 s32, s42, 15
	v_readlane_b32 s46, v254, 43
	v_readlane_b32 s47, v254, 44
	s_cmp_lg_u32 s36, 0
	s_cselect_b32 s46, s40, s46
	s_cselect_b32 s47, s41, s47
	s_lshl_b32 s33, s31, 20
	s_add_i32 s33, s33, s30
	s_lshl_b32 s37, s32, 9
	s_add_i32 s33, s33, s37
	s_add_u32 s46, s46, s33
	s_addc_u32 s47, s47, 0
	v_readlane_b32 s44, v254, 25
	v_readlane_b32 s45, v254, 26
	s_lshl_b32 s33, s32, 20
	s_add_i32 s33, s33, s30
	s_lshl_b32 s37, s36, 19
	s_add_i32 s33, s33, s37
	s_lshl_b32 s37, s31, 8
	s_add_i32 s33, s33, s37
	s_add_u32 s44, s44, s33
	s_addc_u32 s45, s45, 0
	global_load_dwordx4 v[128:131], v105, s[26:27]
	global_load_dwordx4 v[132:135], v106, s[26:27]
	global_load_dwordx4 v[136:139], v107, s[26:27]
	global_load_dwordx4 v[140:143], v108, s[26:27]
	global_load_dwordx4 v[144:147], v109, s[26:27]
	global_load_dwordx4 v[148:151], v110, s[26:27]
	global_load_dwordx4 v[152:155], v111, s[26:27]
	global_load_dwordx4 v[156:159], v112, s[26:27]
	global_load_dwordx4 v[176:179], v105, s[46:47]
	global_load_dwordx4 v[180:183], v106, s[46:47]
	global_load_dwordx4 v[184:187], v107, s[46:47]
	global_load_dwordx4 v[188:191], v108, s[46:47]
	global_load_dwordx4 v[192:195], v109, s[46:47]
	global_load_dwordx4 v[196:199], v110, s[46:47]
	global_load_dwordx4 v[200:203], v111, s[46:47]
	global_load_dwordx4 v[204:207], v112, s[46:47]
	s_waitcnt vmcnt(15)
	ds_write_b32 v113, v128
	ds_write_b32 v113, v129 offset:4
	ds_write_b32 v113, v130 offset:8
	ds_write_b32 v113, v131 offset:12
	s_waitcnt vmcnt(14)
	ds_write_b32 v113, v132 offset:8256
	ds_write_b32 v113, v133 offset:8260
	ds_write_b32 v113, v134 offset:8264
	ds_write_b32 v113, v135 offset:8268
	s_waitcnt vmcnt(13)
	ds_write_b32 v113, v136 offset:16512
	ds_write_b32 v113, v137 offset:16516
	ds_write_b32 v113, v138 offset:16520
	ds_write_b32 v113, v139 offset:16524
	s_waitcnt vmcnt(12)
	ds_write_b32 v113, v140 offset:24768
	ds_write_b32 v113, v141 offset:24772
	ds_write_b32 v113, v142 offset:24776
	ds_write_b32 v113, v143 offset:24780
	s_waitcnt vmcnt(11)
	ds_write_b32 v113, v144 offset:33024
	ds_write_b32 v113, v145 offset:33028
	ds_write_b32 v113, v146 offset:33032
	ds_write_b32 v113, v147 offset:33036
	s_waitcnt vmcnt(10)
	ds_write_b32 v113, v148 offset:41280
	ds_write_b32 v113, v149 offset:41284
	ds_write_b32 v113, v150 offset:41288
	ds_write_b32 v113, v151 offset:41292
	s_waitcnt vmcnt(9)
	ds_write_b32 v113, v152 offset:49536
	ds_write_b32 v113, v153 offset:49540
	ds_write_b32 v113, v154 offset:49544
	ds_write_b32 v113, v155 offset:49548
	s_waitcnt vmcnt(8)
	ds_write_b32 v113, v156 offset:57792
	ds_write_b32 v113, v157 offset:57796
	ds_write_b32 v113, v158 offset:57800
	ds_write_b32 v113, v159 offset:57804
	s_waitcnt vmcnt(7)
	ds_write_b32 v209, v176
	ds_write_b32 v209, v177 offset:4
	ds_write_b32 v209, v178 offset:8
	ds_write_b32 v209, v179 offset:12
	s_waitcnt vmcnt(6)
	ds_write_b32 v209, v180 offset:8256
	ds_write_b32 v209, v181 offset:8260
	ds_write_b32 v209, v182 offset:8264
	ds_write_b32 v209, v183 offset:8268
	s_waitcnt vmcnt(5)
	ds_write_b32 v209, v184 offset:16512
	ds_write_b32 v209, v185 offset:16516
	ds_write_b32 v209, v186 offset:16520
	ds_write_b32 v209, v187 offset:16524
	s_waitcnt vmcnt(4)
	ds_write_b32 v209, v188 offset:24768
	ds_write_b32 v209, v189 offset:24772
	ds_write_b32 v209, v190 offset:24776
	ds_write_b32 v209, v191 offset:24780
	s_waitcnt vmcnt(3)
	ds_write_b32 v209, v192 offset:33024
	ds_write_b32 v209, v193 offset:33028
	ds_write_b32 v209, v194 offset:33032
	ds_write_b32 v209, v195 offset:33036
	s_waitcnt vmcnt(2)
	ds_write_b32 v209, v196 offset:41280
	ds_write_b32 v209, v197 offset:41284
	ds_write_b32 v209, v198 offset:41288
	ds_write_b32 v209, v199 offset:41292
	s_waitcnt vmcnt(1)
	ds_write_b32 v209, v200 offset:49536
	ds_write_b32 v209, v201 offset:49540
	ds_write_b32 v209, v202 offset:49544
	ds_write_b32 v209, v203 offset:49548
	s_waitcnt vmcnt(0)
	ds_write_b32 v209, v204 offset:57792
	ds_write_b32 v209, v205 offset:57796
	ds_write_b32 v209, v206 offset:57800
	ds_write_b32 v209, v207 offset:57804
	s_waitcnt lgkmcnt(0)
	s_barrier
; #define LAS __attribute__((address_space(3)))
; __device__ __forceinline__ void lds_barrier() { asm volatile("s_waitcnt lgkmcnt(0)" ::: "memory"); __builtin_amdgcn_s_barrier(); asm volatile("" ::: "memory"); }
; __device__ __forceinline__ unsigned xb_add(unsigned* p, unsigned v) { return __hip_atomic_fetch_add(p, v, __ATOMIC_RELAXED, __HIP_MEMORY_SCOPE_AGENT); }
; __device__ __forceinline__ void phase_prologue(const Args& a, LAS unsigned char* lds) {
;     ...
;         lds_barrier();
; #pragma unroll
;         for (int i = 0; i < 4; ++i) { const int piece = tid + 512 * i, nl = piece >> 4, kg = piece & 15; const LAS float* s = tile + (kg * 8) * 129 + nl;
;             u32x4 o; o.x = pk2(s[0], s[129]); o.y = pk2(s[258], s[387]); o.z = pk2(s[516], s[645]); o.w = pk2(s[774], s[903]);
;             *(u32x4*)(dst + (size_t)(drow0 + nl) * 2048 + k0 + kg * 8) = o; }
;         ++it;
;         if (tid == 0) { qs[it & 1] = pend; pend = (int)xb_add(cq_head, 1u); }
;         lds_barrier();
	ds_read_b32 v160, v114
	ds_read_b32 v161, v114 offset:516
	ds_read_b32 v162, v114 offset:1032
	ds_read_b32 v163, v114 offset:1548
	ds_read_b32 v164, v114 offset:2064
	ds_read_b32 v165, v114 offset:2580
	ds_read_b32 v166, v114 offset:3096
	ds_read_b32 v167, v114 offset:3612
	s_waitcnt lgkmcnt(0)
	v_cvt_pk_bf16_f32 v168, v160, v161
	v_cvt_pk_bf16_f32 v169, v162, v163
	v_cvt_pk_bf16_f32 v170, v164, v165
	v_cvt_pk_bf16_f32 v171, v166, v167
	global_store_dwordx4 v115, v[168:171], s[28:29]
	ds_read_b32 v160, v114 offset:128
	ds_read_b32 v161, v114 offset:644
	ds_read_b32 v162, v114 offset:1160
	ds_read_b32 v163, v114 offset:1676
	ds_read_b32 v164, v114 offset:2192
	ds_read_b32 v165, v114 offset:2708
	ds_read_b32 v166, v114 offset:3224
	ds_read_b32 v167, v114 offset:3740
	s_waitcnt lgkmcnt(0)
	v_cvt_pk_bf16_f32 v172, v160, v161
	v_cvt_pk_bf16_f32 v173, v162, v163
	v_cvt_pk_bf16_f32 v174, v164, v165
	v_cvt_pk_bf16_f32 v175, v166, v167
	global_store_dwordx4 v116, v[172:175], s[28:29]
	ds_read_b32 v160, v114 offset:256
	ds_read_b32 v161, v114 offset:772
	ds_read_b32 v162, v114 offset:1288
	ds_read_b32 v163, v114 offset:1804
	ds_read_b32 v164, v114 offset:2320
	ds_read_b32 v165, v114 offset:2836
	ds_read_b32 v166, v114 offset:3352
	ds_read_b32 v167, v114 offset:3868
	s_waitcnt lgkmcnt(0)
	v_cvt_pk_bf16_f32 v168, v160, v161
	v_cvt_pk_bf16_f32 v169, v162, v163
	v_cvt_pk_bf16_f32 v170, v164, v165
	v_cvt_pk_bf16_f32 v171, v166, v167
	global_store_dwordx4 v117, v[168:171], s[28:29]
	ds_read_b32 v160, v114 offset:384
	ds_read_b32 v161, v114 offset:900
	ds_read_b32 v162, v114 offset:1416
	ds_read_b32 v163, v114 offset:1932
	ds_read_b32 v164, v114 offset:2448
	ds_read_b32 v165, v114 offset:2964
	ds_read_b32 v166, v114 offset:3480
	ds_read_b32 v167, v114 offset:3996
	s_waitcnt lgkmcnt(0)
	v_cvt_pk_bf16_f32 v172, v160, v161
	v_cvt_pk_bf16_f32 v173, v162, v163
	v_cvt_pk_bf16_f32 v174, v164, v165
	v_cvt_pk_bf16_f32 v175, v166, v167
	global_store_dwordx4 v118, v[172:175], s[28:29]
	ds_read_b32 v160, v210
	ds_read_b32 v161, v210 offset:516
	ds_read_b32 v162, v210 offset:1032
	ds_read_b32 v163, v210 offset:1548
	ds_read_b32 v164, v210 offset:2064
	ds_read_b32 v165, v210 offset:2580
	ds_read_b32 v166, v210 offset:3096
	ds_read_b32 v167, v210 offset:3612
	s_waitcnt lgkmcnt(0)
	v_cvt_pk_bf16_f32 v168, v160, v161
	v_cvt_pk_bf16_f32 v169, v162, v163
	v_cvt_pk_bf16_f32 v170, v164, v165
	v_cvt_pk_bf16_f32 v171, v166, v167
	global_store_dwordx4 v115, v[168:171], s[44:45]
	ds_read_b32 v160, v210 offset:128
	ds_read_b32 v161, v210 offset:644
	ds_read_b32 v162, v210 offset:1160
	ds_read_b32 v163, v210 offset:1676
	ds_read_b32 v164, v210 offset:2192
	ds_read_b32 v165, v210 offset:2708
	ds_read_b32 v166, v210 offset:3224
	ds_read_b32 v167, v210 offset:3740
	s_waitcnt lgkmcnt(0)
	v_cvt_pk_bf16_f32 v172, v160, v161
	v_cvt_pk_bf16_f32 v173, v162, v163
	v_cvt_pk_bf16_f32 v174, v164, v165
	v_cvt_pk_bf16_f32 v175, v166, v167
	global_store_dwordx4 v116, v[172:175], s[44:45]
	ds_read_b32 v160, v210 offset:256
	ds_read_b32 v161, v210 offset:772
	ds_read_b32 v162, v210 offset:1288
	ds_read_b32 v163, v210 offset:1804
	ds_read_b32 v164, v210 offset:2320
	ds_read_b32 v165, v210 offset:2836
	ds_read_b32 v166, v210 offset:3352
	ds_read_b32 v167, v210 offset:3868
	s_waitcnt lgkmcnt(0)
	v_cvt_pk_bf16_f32 v168, v160, v161
	v_cvt_pk_bf16_f32 v169, v162, v163
	v_cvt_pk_bf16_f32 v170, v164, v165
	v_cvt_pk_bf16_f32 v171, v166, v167
	global_store_dwordx4 v117, v[168:171], s[44:45]
	ds_read_b32 v160, v210 offset:384
	ds_read_b32 v161, v210 offset:900
	ds_read_b32 v162, v210 offset:1416
	ds_read_b32 v163, v210 offset:1932
	ds_read_b32 v164, v210 offset:2448
	ds_read_b32 v165, v210 offset:2964
	ds_read_b32 v166, v210 offset:3480
	ds_read_b32 v167, v210 offset:3996
	s_waitcnt lgkmcnt(0)
	v_cvt_pk_bf16_f32 v172, v160, v161
	v_cvt_pk_bf16_f32 v173, v162, v163
	v_cvt_pk_bf16_f32 v174, v164, v165
	v_cvt_pk_bf16_f32 v175, v166, v167
	global_store_dwordx4 v118, v[172:175], s[44:45]
	v_cmp_eq_u32_e32 vcc, 0, v0
	s_and_saveexec_b64 s[34:35], vcc
	s_cbranch_execz .Lcvz_t0c
	s_waitcnt vmcnt(0)
	ds_write_b32 v125, v123
